# retention state scan: chunk loads prefetched 8 steps ahead with counted waits (was about one load in flight per wave)
# speedup vs baseline: 1.0123x; 1.0058x over previous
; #define GAS __attribute__((address_space(1)))
; __device__ __forceinline__ unsigned cvt_pk_bf16(float lo, float hi) { unsigned r; asm volatile("v_cvt_pk_bf16_f32 %0, %1, %2" : "=v"(r) : "v"(lo), "v"(hi)); return r; }
; __device__ __forceinline__ float fexp(float x) { return __builtin_amdgcn_exp2f(x * 1.4426950408889634f); }
; __device__ __forceinline__ void p3_scan(Frame& F) {
;     ...
;     for (int q = F.vcu * NTHR + FTID; q < NQ; q += F.G * NTHR) {
;         const int dk4 = q & 63, dv = (q >> 6) & 255, dh = q >> 14, dir = dh >> 2, h = dh & 3;
;         const float lg = -fexp((dir ? F.dec_b : F.dec_f)[h]); const float cd = fexp(lg * (float)C2);
;         f32x4 S = (f32x4){0.f, 0.f, 0.f, 0.f};
;         for (int s = 0; s < NCH; ++s) { const int n = dir ? (NCH - 1 - s) : s;
;             const v2u kw = *(const GAS v2u*)(kvT + (((size_t)dh * NCH + n) * 256 + dv) * 256 + dk4 * 4); const f32x4 kv = (f32x4){bf_lo(kw.x), bf_hi(kw.x), bf_lo(kw.y), bf_hi(kw.y)};
;             v2u w; w.x = cvt_pk_bf16(S[0], S[1]); w.y = cvt_pk_bf16(S[2], S[3]);
;             *(GAS v2u*)(Bcat + ((size_t)(h * NCH + n) * 256 + dv) * CAT + 256 + dir * 256 + dk4 * 4) = w;
;             S = S * cd + kv; }
;     }
.LBB0_832:
	v_mov_b32_e32 v196, 0x20000
	v_mov_b32_e32 v198, 0xfffe0000
	v_cndmask_b32_e32 v196, v198, v196, vcc
	v_cndmask_b32_e64 v197, -1, 0, vcc
	v_mov_b32_e32 v199, 0x60000
	v_mov_b32_e32 v200, 0xfffa0000
	v_cndmask_b32_e32 v198, v200, v199, vcc
	v_mov_b32_e32 v199, v197
	v_cndmask_b32_e64 v200, 63, 0, vcc
	v_lshlrev_b32_e32 v202, 8, v200
	v_mov_b32_e32 v203, 0
	v_lshl_add_u64 v[202:203], v[4:5], 0, v[202:203]
	v_lshlrev_b64 v[202:203], 9, v[202:203]
	v_lshl_add_u64 v[202:203], v[10:11], 0, v[202:203]
	v_lshl_add_u32 v204, v200, 8, v23
	v_mul_lo_u32 v204, v204, s14
	v_mov_b32_e32 v205, 0
	v_lshl_add_u64 v[204:205], v[204:205], 1, s[28:29]
	v_lshl_add_u64 v[204:205], v[204:205], 0, v[8:9]
	v_lshl_add_u64 v[204:205], v[204:205], 0, v[2:3]
	s_mov_b32 s4, s15
	s_mov_b32 s5, 0
	v_lshl_add_u64 v[204:205], v[204:205], 0, s[4:5]
	global_load_dwordx2 v[206:207], v[202:203], off
	v_lshl_add_u64 v[202:203], v[202:203], 0, v[196:197]
	global_load_dwordx2 v[208:209], v[202:203], off
	v_lshl_add_u64 v[202:203], v[202:203], 0, v[196:197]
	global_load_dwordx2 v[210:211], v[202:203], off
	v_lshl_add_u64 v[202:203], v[202:203], 0, v[196:197]
	global_load_dwordx2 v[212:213], v[202:203], off
	v_lshl_add_u64 v[202:203], v[202:203], 0, v[196:197]
	global_load_dwordx2 v[214:215], v[202:203], off
	v_lshl_add_u64 v[202:203], v[202:203], 0, v[196:197]
	global_load_dwordx2 v[216:217], v[202:203], off
	v_lshl_add_u64 v[202:203], v[202:203], 0, v[196:197]
	global_load_dwordx2 v[218:219], v[202:203], off
	v_lshl_add_u64 v[202:203], v[202:203], 0, v[196:197]
	global_load_dwordx2 v[220:221], v[202:203], off
	v_lshl_add_u64 v[202:203], v[202:203], 0, v[196:197]
	s_waitcnt vmcnt(7)
	v_cvt_pk_bf16_f32 v222, v14, v15
	v_cvt_pk_bf16_f32 v223, v16, v17
	global_store_dwordx2 v[204:205], v[222:223], off offset:512
	v_lshl_add_u64 v[204:205], v[204:205], 0, v[198:199]
	v_lshlrev_b32_e32 v224, 16, v206
	v_and_b32_e32 v225, 0xffff0000, v206
	v_lshlrev_b32_e32 v226, 16, v207
	v_and_b32_e32 v227, 0xffff0000, v207
	v_pk_fma_f32 v[14:15], v[6:7], v[14:15], v[224:225]
	v_pk_fma_f32 v[16:17], v[12:13], v[16:17], v[226:227]
	global_load_dwordx2 v[206:207], v[202:203], off
	v_lshl_add_u64 v[202:203], v[202:203], 0, v[196:197]
	s_waitcnt vmcnt(8)
	v_cvt_pk_bf16_f32 v222, v14, v15
	v_cvt_pk_bf16_f32 v223, v16, v17
	global_store_dwordx2 v[204:205], v[222:223], off offset:512
	v_lshl_add_u64 v[204:205], v[204:205], 0, v[198:199]
	v_lshlrev_b32_e32 v224, 16, v208
	v_and_b32_e32 v225, 0xffff0000, v208
	v_lshlrev_b32_e32 v226, 16, v209
	v_and_b32_e32 v227, 0xffff0000, v209
	v_pk_fma_f32 v[14:15], v[6:7], v[14:15], v[224:225]
	v_pk_fma_f32 v[16:17], v[12:13], v[16:17], v[226:227]
	global_load_dwordx2 v[208:209], v[202:203], off
	v_lshl_add_u64 v[202:203], v[202:203], 0, v[196:197]
	s_waitcnt vmcnt(9)
	v_cvt_pk_bf16_f32 v222, v14, v15
	v_cvt_pk_bf16_f32 v223, v16, v17
	global_store_dwordx2 v[204:205], v[222:223], off offset:512
	v_lshl_add_u64 v[204:205], v[204:205], 0, v[198:199]
	v_lshlrev_b32_e32 v224, 16, v210
	v_and_b32_e32 v225, 0xffff0000, v210
	v_lshlrev_b32_e32 v226, 16, v211
	v_and_b32_e32 v227, 0xffff0000, v211
	v_pk_fma_f32 v[14:15], v[6:7], v[14:15], v[224:225]
	v_pk_fma_f32 v[16:17], v[12:13], v[16:17], v[226:227]
	global_load_dwordx2 v[210:211], v[202:203], off
	v_lshl_add_u64 v[202:203], v[202:203], 0, v[196:197]
	s_waitcnt vmcnt(10)
	v_cvt_pk_bf16_f32 v222, v14, v15
	v_cvt_pk_bf16_f32 v223, v16, v17
	global_store_dwordx2 v[204:205], v[222:223], off offset:512
	v_lshl_add_u64 v[204:205], v[204:205], 0, v[198:199]
	v_lshlrev_b32_e32 v224, 16, v212
	v_and_b32_e32 v225, 0xffff0000, v212
	v_lshlrev_b32_e32 v226, 16, v213
	v_and_b32_e32 v227, 0xffff0000, v213
	v_pk_fma_f32 v[14:15], v[6:7], v[14:15], v[224:225]
	v_pk_fma_f32 v[16:17], v[12:13], v[16:17], v[226:227]
	global_load_dwordx2 v[212:213], v[202:203], off
	v_lshl_add_u64 v[202:203], v[202:203], 0, v[196:197]
	s_waitcnt vmcnt(11)
	v_cvt_pk_bf16_f32 v222, v14, v15
	v_cvt_pk_bf16_f32 v223, v16, v17
	global_store_dwordx2 v[204:205], v[222:223], off offset:512
	v_lshl_add_u64 v[204:205], v[204:205], 0, v[198:199]
	v_lshlrev_b32_e32 v224, 16, v214
	v_and_b32_e32 v225, 0xffff0000, v214
	v_lshlrev_b32_e32 v226, 16, v215
	v_and_b32_e32 v227, 0xffff0000, v215
	v_pk_fma_f32 v[14:15], v[6:7], v[14:15], v[224:225]
	v_pk_fma_f32 v[16:17], v[12:13], v[16:17], v[226:227]
	global_load_dwordx2 v[214:215], v[202:203], off
	v_lshl_add_u64 v[202:203], v[202:203], 0, v[196:197]
	s_waitcnt vmcnt(12)
	v_cvt_pk_bf16_f32 v222, v14, v15
	v_cvt_pk_bf16_f32 v223, v16, v17
	global_store_dwordx2 v[204:205], v[222:223], off offset:512
	v_lshl_add_u64 v[204:205], v[204:205], 0, v[198:199]
	v_lshlrev_b32_e32 v224, 16, v216
	v_and_b32_e32 v225, 0xffff0000, v216
	v_lshlrev_b32_e32 v226, 16, v217
	v_and_b32_e32 v227, 0xffff0000, v217
	v_pk_fma_f32 v[14:15], v[6:7], v[14:15], v[224:225]
	v_pk_fma_f32 v[16:17], v[12:13], v[16:17], v[226:227]
	global_load_dwordx2 v[216:217], v[202:203], off
	v_lshl_add_u64 v[202:203], v[202:203], 0, v[196:197]
	s_waitcnt vmcnt(13)
	v_cvt_pk_bf16_f32 v222, v14, v15
	v_cvt_pk_bf16_f32 v223, v16, v17
	global_store_dwordx2 v[204:205], v[222:223], off offset:512
	v_lshl_add_u64 v[204:205], v[204:205], 0, v[198:199]
	v_lshlrev_b32_e32 v224, 16, v218
	v_and_b32_e32 v225, 0xffff0000, v218
	v_lshlrev_b32_e32 v226, 16, v219
	v_and_b32_e32 v227, 0xffff0000, v219
	v_pk_fma_f32 v[14:15], v[6:7], v[14:15], v[224:225]
	v_pk_fma_f32 v[16:17], v[12:13], v[16:17], v[226:227]
	global_load_dwordx2 v[218:219], v[202:203], off
	v_lshl_add_u64 v[202:203], v[202:203], 0, v[196:197]
	s_waitcnt vmcnt(14)
; #define GAS __attribute__((address_space(1)))
; __device__ __forceinline__ unsigned cvt_pk_bf16(float lo, float hi) { unsigned r; asm volatile("v_cvt_pk_bf16_f32 %0, %1, %2" : "=v"(r) : "v"(lo), "v"(hi)); return r; }
; __device__ __forceinline__ void p3_scan(Frame& F) {
;     ...
;         for (int s = 0; s < NCH; ++s) { const int n = dir ? (NCH - 1 - s) : s;
;             const v2u kw = *(const GAS v2u*)(kvT + (((size_t)dh * NCH + n) * 256 + dv) * 256 + dk4 * 4); const f32x4 kv = (f32x4){bf_lo(kw.x), bf_hi(kw.x), bf_lo(kw.y), bf_hi(kw.y)};
;             v2u w; w.x = cvt_pk_bf16(S[0], S[1]); w.y = cvt_pk_bf16(S[2], S[3]);
;             *(GAS v2u*)(Bcat + ((size_t)(h * NCH + n) * 256 + dv) * CAT + 256 + dir * 256 + dk4 * 4) = w;
;             S = S * cd + kv; }
	v_cvt_pk_bf16_f32 v222, v14, v15
	v_cvt_pk_bf16_f32 v223, v16, v17
	global_store_dwordx2 v[204:205], v[222:223], off offset:512
	v_lshl_add_u64 v[204:205], v[204:205], 0, v[198:199]
	v_lshlrev_b32_e32 v224, 16, v220
	v_and_b32_e32 v225, 0xffff0000, v220
	v_lshlrev_b32_e32 v226, 16, v221
	v_and_b32_e32 v227, 0xffff0000, v221
	v_pk_fma_f32 v[14:15], v[6:7], v[14:15], v[224:225]
	v_pk_fma_f32 v[16:17], v[12:13], v[16:17], v[226:227]
	global_load_dwordx2 v[220:221], v[202:203], off
	v_lshl_add_u64 v[202:203], v[202:203], 0, v[196:197]
	s_waitcnt vmcnt(14)
	v_cvt_pk_bf16_f32 v222, v14, v15
	v_cvt_pk_bf16_f32 v223, v16, v17
	global_store_dwordx2 v[204:205], v[222:223], off offset:512
	v_lshl_add_u64 v[204:205], v[204:205], 0, v[198:199]
	v_lshlrev_b32_e32 v224, 16, v206
	v_and_b32_e32 v225, 0xffff0000, v206
	v_lshlrev_b32_e32 v226, 16, v207
	v_and_b32_e32 v227, 0xffff0000, v207
	v_pk_fma_f32 v[14:15], v[6:7], v[14:15], v[224:225]
	v_pk_fma_f32 v[16:17], v[12:13], v[16:17], v[226:227]
	global_load_dwordx2 v[206:207], v[202:203], off
	v_lshl_add_u64 v[202:203], v[202:203], 0, v[196:197]
	s_waitcnt vmcnt(14)
	v_cvt_pk_bf16_f32 v222, v14, v15
	v_cvt_pk_bf16_f32 v223, v16, v17
	global_store_dwordx2 v[204:205], v[222:223], off offset:512
	v_lshl_add_u64 v[204:205], v[204:205], 0, v[198:199]
	v_lshlrev_b32_e32 v224, 16, v208
	v_and_b32_e32 v225, 0xffff0000, v208
	v_lshlrev_b32_e32 v226, 16, v209
	v_and_b32_e32 v227, 0xffff0000, v209
	v_pk_fma_f32 v[14:15], v[6:7], v[14:15], v[224:225]
	v_pk_fma_f32 v[16:17], v[12:13], v[16:17], v[226:227]
	global_load_dwordx2 v[208:209], v[202:203], off
	v_lshl_add_u64 v[202:203], v[202:203], 0, v[196:197]
	s_waitcnt vmcnt(14)
	v_cvt_pk_bf16_f32 v222, v14, v15
	v_cvt_pk_bf16_f32 v223, v16, v17
	global_store_dwordx2 v[204:205], v[222:223], off offset:512
	v_lshl_add_u64 v[204:205], v[204:205], 0, v[198:199]
	v_lshlrev_b32_e32 v224, 16, v210
	v_and_b32_e32 v225, 0xffff0000, v210
	v_lshlrev_b32_e32 v226, 16, v211
	v_and_b32_e32 v227, 0xffff0000, v211
	v_pk_fma_f32 v[14:15], v[6:7], v[14:15], v[224:225]
	v_pk_fma_f32 v[16:17], v[12:13], v[16:17], v[226:227]
	global_load_dwordx2 v[210:211], v[202:203], off
	v_lshl_add_u64 v[202:203], v[202:203], 0, v[196:197]
	s_waitcnt vmcnt(14)
	v_cvt_pk_bf16_f32 v222, v14, v15
	v_cvt_pk_bf16_f32 v223, v16, v17
	global_store_dwordx2 v[204:205], v[222:223], off offset:512
	v_lshl_add_u64 v[204:205], v[204:205], 0, v[198:199]
	v_lshlrev_b32_e32 v224, 16, v212
	v_and_b32_e32 v225, 0xffff0000, v212
	v_lshlrev_b32_e32 v226, 16, v213
	v_and_b32_e32 v227, 0xffff0000, v213
	v_pk_fma_f32 v[14:15], v[6:7], v[14:15], v[224:225]
	v_pk_fma_f32 v[16:17], v[12:13], v[16:17], v[226:227]
	global_load_dwordx2 v[212:213], v[202:203], off
	v_lshl_add_u64 v[202:203], v[202:203], 0, v[196:197]
	s_waitcnt vmcnt(14)
	v_cvt_pk_bf16_f32 v222, v14, v15
	v_cvt_pk_bf16_f32 v223, v16, v17
	global_store_dwordx2 v[204:205], v[222:223], off offset:512
	v_lshl_add_u64 v[204:205], v[204:205], 0, v[198:199]
	v_lshlrev_b32_e32 v224, 16, v214
	v_and_b32_e32 v225, 0xffff0000, v214
	v_lshlrev_b32_e32 v226, 16, v215
	v_and_b32_e32 v227, 0xffff0000, v215
	v_pk_fma_f32 v[14:15], v[6:7], v[14:15], v[224:225]
	v_pk_fma_f32 v[16:17], v[12:13], v[16:17], v[226:227]
	global_load_dwordx2 v[214:215], v[202:203], off
	v_lshl_add_u64 v[202:203], v[202:203], 0, v[196:197]
	s_waitcnt vmcnt(14)
	v_cvt_pk_bf16_f32 v222, v14, v15
	v_cvt_pk_bf16_f32 v223, v16, v17
	global_store_dwordx2 v[204:205], v[222:223], off offset:512
	v_lshl_add_u64 v[204:205], v[204:205], 0, v[198:199]
	v_lshlrev_b32_e32 v224, 16, v216
	v_and_b32_e32 v225, 0xffff0000, v216
	v_lshlrev_b32_e32 v226, 16, v217
	v_and_b32_e32 v227, 0xffff0000, v217
	v_pk_fma_f32 v[14:15], v[6:7], v[14:15], v[224:225]
	v_pk_fma_f32 v[16:17], v[12:13], v[16:17], v[226:227]
	global_load_dwordx2 v[216:217], v[202:203], off
	v_lshl_add_u64 v[202:203], v[202:203], 0, v[196:197]
	s_waitcnt vmcnt(14)
	v_cvt_pk_bf16_f32 v222, v14, v15
	v_cvt_pk_bf16_f32 v223, v16, v17
	global_store_dwordx2 v[204:205], v[222:223], off offset:512
	v_lshl_add_u64 v[204:205], v[204:205], 0, v[198:199]
	v_lshlrev_b32_e32 v224, 16, v218
	v_and_b32_e32 v225, 0xffff0000, v218
	v_lshlrev_b32_e32 v226, 16, v219
	v_and_b32_e32 v227, 0xffff0000, v219
	v_pk_fma_f32 v[14:15], v[6:7], v[14:15], v[224:225]
	v_pk_fma_f32 v[16:17], v[12:13], v[16:17], v[226:227]
	global_load_dwordx2 v[218:219], v[202:203], off
	v_lshl_add_u64 v[202:203], v[202:203], 0, v[196:197]
	s_waitcnt vmcnt(14)
	v_cvt_pk_bf16_f32 v222, v14, v15
	v_cvt_pk_bf16_f32 v223, v16, v17
	global_store_dwordx2 v[204:205], v[222:223], off offset:512
	v_lshl_add_u64 v[204:205], v[204:205], 0, v[198:199]
	v_lshlrev_b32_e32 v224, 16, v220
	v_and_b32_e32 v225, 0xffff0000, v220
	v_lshlrev_b32_e32 v226, 16, v221
	v_and_b32_e32 v227, 0xffff0000, v221
	v_pk_fma_f32 v[14:15], v[6:7], v[14:15], v[224:225]
	v_pk_fma_f32 v[16:17], v[12:13], v[16:17], v[226:227]
	global_load_dwordx2 v[220:221], v[202:203], off
	v_lshl_add_u64 v[202:203], v[202:203], 0, v[196:197]
	s_waitcnt vmcnt(14)
	v_cvt_pk_bf16_f32 v222, v14, v15
	v_cvt_pk_bf16_f32 v223, v16, v17
	global_store_dwordx2 v[204:205], v[222:223], off offset:512
	v_lshl_add_u64 v[204:205], v[204:205], 0, v[198:199]
	v_lshlrev_b32_e32 v224, 16, v206
	v_and_b32_e32 v225, 0xffff0000, v206
	v_lshlrev_b32_e32 v226, 16, v207
	v_and_b32_e32 v227, 0xffff0000, v207
	v_pk_fma_f32 v[14:15], v[6:7], v[14:15], v[224:225]
	v_pk_fma_f32 v[16:17], v[12:13], v[16:17], v[226:227]
	global_load_dwordx2 v[206:207], v[202:203], off
	v_lshl_add_u64 v[202:203], v[202:203], 0, v[196:197]
	s_waitcnt vmcnt(14)
; #define GAS __attribute__((address_space(1)))
; __device__ __forceinline__ unsigned cvt_pk_bf16(float lo, float hi) { unsigned r; asm volatile("v_cvt_pk_bf16_f32 %0, %1, %2" : "=v"(r) : "v"(lo), "v"(hi)); return r; }
; __device__ __forceinline__ void p3_scan(Frame& F) {
;     ...
;         for (int s = 0; s < NCH; ++s) { const int n = dir ? (NCH - 1 - s) : s;
;             const v2u kw = *(const GAS v2u*)(kvT + (((size_t)dh * NCH + n) * 256 + dv) * 256 + dk4 * 4); const f32x4 kv = (f32x4){bf_lo(kw.x), bf_hi(kw.x), bf_lo(kw.y), bf_hi(kw.y)};
;             v2u w; w.x = cvt_pk_bf16(S[0], S[1]); w.y = cvt_pk_bf16(S[2], S[3]);
;             *(GAS v2u*)(Bcat + ((size_t)(h * NCH + n) * 256 + dv) * CAT + 256 + dir * 256 + dk4 * 4) = w;
;             S = S * cd + kv; }
	v_cvt_pk_bf16_f32 v222, v14, v15
	v_cvt_pk_bf16_f32 v223, v16, v17
	global_store_dwordx2 v[204:205], v[222:223], off offset:512
	v_lshl_add_u64 v[204:205], v[204:205], 0, v[198:199]
	v_lshlrev_b32_e32 v224, 16, v208
	v_and_b32_e32 v225, 0xffff0000, v208
	v_lshlrev_b32_e32 v226, 16, v209
	v_and_b32_e32 v227, 0xffff0000, v209
	v_pk_fma_f32 v[14:15], v[6:7], v[14:15], v[224:225]
	v_pk_fma_f32 v[16:17], v[12:13], v[16:17], v[226:227]
	global_load_dwordx2 v[208:209], v[202:203], off
	v_lshl_add_u64 v[202:203], v[202:203], 0, v[196:197]
	s_waitcnt vmcnt(14)
	v_cvt_pk_bf16_f32 v222, v14, v15
	v_cvt_pk_bf16_f32 v223, v16, v17
	global_store_dwordx2 v[204:205], v[222:223], off offset:512
	v_lshl_add_u64 v[204:205], v[204:205], 0, v[198:199]
	v_lshlrev_b32_e32 v224, 16, v210
	v_and_b32_e32 v225, 0xffff0000, v210
	v_lshlrev_b32_e32 v226, 16, v211
	v_and_b32_e32 v227, 0xffff0000, v211
	v_pk_fma_f32 v[14:15], v[6:7], v[14:15], v[224:225]
	v_pk_fma_f32 v[16:17], v[12:13], v[16:17], v[226:227]
	global_load_dwordx2 v[210:211], v[202:203], off
	v_lshl_add_u64 v[202:203], v[202:203], 0, v[196:197]
	s_waitcnt vmcnt(14)
	v_cvt_pk_bf16_f32 v222, v14, v15
	v_cvt_pk_bf16_f32 v223, v16, v17
	global_store_dwordx2 v[204:205], v[222:223], off offset:512
	v_lshl_add_u64 v[204:205], v[204:205], 0, v[198:199]
	v_lshlrev_b32_e32 v224, 16, v212
	v_and_b32_e32 v225, 0xffff0000, v212
	v_lshlrev_b32_e32 v226, 16, v213
	v_and_b32_e32 v227, 0xffff0000, v213
	v_pk_fma_f32 v[14:15], v[6:7], v[14:15], v[224:225]
	v_pk_fma_f32 v[16:17], v[12:13], v[16:17], v[226:227]
	global_load_dwordx2 v[212:213], v[202:203], off
	v_lshl_add_u64 v[202:203], v[202:203], 0, v[196:197]
	s_waitcnt vmcnt(14)
	v_cvt_pk_bf16_f32 v222, v14, v15
	v_cvt_pk_bf16_f32 v223, v16, v17
	global_store_dwordx2 v[204:205], v[222:223], off offset:512
	v_lshl_add_u64 v[204:205], v[204:205], 0, v[198:199]
	v_lshlrev_b32_e32 v224, 16, v214
	v_and_b32_e32 v225, 0xffff0000, v214
	v_lshlrev_b32_e32 v226, 16, v215
	v_and_b32_e32 v227, 0xffff0000, v215
	v_pk_fma_f32 v[14:15], v[6:7], v[14:15], v[224:225]
	v_pk_fma_f32 v[16:17], v[12:13], v[16:17], v[226:227]
	global_load_dwordx2 v[214:215], v[202:203], off
	v_lshl_add_u64 v[202:203], v[202:203], 0, v[196:197]
	s_waitcnt vmcnt(14)
	v_cvt_pk_bf16_f32 v222, v14, v15
	v_cvt_pk_bf16_f32 v223, v16, v17
	global_store_dwordx2 v[204:205], v[222:223], off offset:512
	v_lshl_add_u64 v[204:205], v[204:205], 0, v[198:199]
	v_lshlrev_b32_e32 v224, 16, v216
	v_and_b32_e32 v225, 0xffff0000, v216
	v_lshlrev_b32_e32 v226, 16, v217
	v_and_b32_e32 v227, 0xffff0000, v217
	v_pk_fma_f32 v[14:15], v[6:7], v[14:15], v[224:225]
	v_pk_fma_f32 v[16:17], v[12:13], v[16:17], v[226:227]
	global_load_dwordx2 v[216:217], v[202:203], off
	v_lshl_add_u64 v[202:203], v[202:203], 0, v[196:197]
	s_waitcnt vmcnt(14)
	v_cvt_pk_bf16_f32 v222, v14, v15
	v_cvt_pk_bf16_f32 v223, v16, v17
	global_store_dwordx2 v[204:205], v[222:223], off offset:512
	v_lshl_add_u64 v[204:205], v[204:205], 0, v[198:199]
	v_lshlrev_b32_e32 v224, 16, v218
	v_and_b32_e32 v225, 0xffff0000, v218
	v_lshlrev_b32_e32 v226, 16, v219
	v_and_b32_e32 v227, 0xffff0000, v219
	v_pk_fma_f32 v[14:15], v[6:7], v[14:15], v[224:225]
	v_pk_fma_f32 v[16:17], v[12:13], v[16:17], v[226:227]
	global_load_dwordx2 v[218:219], v[202:203], off
	v_lshl_add_u64 v[202:203], v[202:203], 0, v[196:197]
	s_waitcnt vmcnt(14)
	v_cvt_pk_bf16_f32 v222, v14, v15
	v_cvt_pk_bf16_f32 v223, v16, v17
	global_store_dwordx2 v[204:205], v[222:223], off offset:512
	v_lshl_add_u64 v[204:205], v[204:205], 0, v[198:199]
	v_lshlrev_b32_e32 v224, 16, v220
	v_and_b32_e32 v225, 0xffff0000, v220
	v_lshlrev_b32_e32 v226, 16, v221
	v_and_b32_e32 v227, 0xffff0000, v221
	v_pk_fma_f32 v[14:15], v[6:7], v[14:15], v[224:225]
	v_pk_fma_f32 v[16:17], v[12:13], v[16:17], v[226:227]
	global_load_dwordx2 v[220:221], v[202:203], off
	v_lshl_add_u64 v[202:203], v[202:203], 0, v[196:197]
	s_waitcnt vmcnt(14)
	v_cvt_pk_bf16_f32 v222, v14, v15
	v_cvt_pk_bf16_f32 v223, v16, v17
	global_store_dwordx2 v[204:205], v[222:223], off offset:512
	v_lshl_add_u64 v[204:205], v[204:205], 0, v[198:199]
	v_lshlrev_b32_e32 v224, 16, v206
	v_and_b32_e32 v225, 0xffff0000, v206
	v_lshlrev_b32_e32 v226, 16, v207
	v_and_b32_e32 v227, 0xffff0000, v207
	v_pk_fma_f32 v[14:15], v[6:7], v[14:15], v[224:225]
	v_pk_fma_f32 v[16:17], v[12:13], v[16:17], v[226:227]
	global_load_dwordx2 v[206:207], v[202:203], off
	v_lshl_add_u64 v[202:203], v[202:203], 0, v[196:197]
	s_waitcnt vmcnt(14)
	v_cvt_pk_bf16_f32 v222, v14, v15
	v_cvt_pk_bf16_f32 v223, v16, v17
	global_store_dwordx2 v[204:205], v[222:223], off offset:512
	v_lshl_add_u64 v[204:205], v[204:205], 0, v[198:199]
	v_lshlrev_b32_e32 v224, 16, v208
	v_and_b32_e32 v225, 0xffff0000, v208
	v_lshlrev_b32_e32 v226, 16, v209
	v_and_b32_e32 v227, 0xffff0000, v209
	v_pk_fma_f32 v[14:15], v[6:7], v[14:15], v[224:225]
	v_pk_fma_f32 v[16:17], v[12:13], v[16:17], v[226:227]
	global_load_dwordx2 v[208:209], v[202:203], off
	v_lshl_add_u64 v[202:203], v[202:203], 0, v[196:197]
	s_waitcnt vmcnt(14)
	v_cvt_pk_bf16_f32 v222, v14, v15
	v_cvt_pk_bf16_f32 v223, v16, v17
	global_store_dwordx2 v[204:205], v[222:223], off offset:512
	v_lshl_add_u64 v[204:205], v[204:205], 0, v[198:199]
	v_lshlrev_b32_e32 v224, 16, v210
	v_and_b32_e32 v225, 0xffff0000, v210
	v_lshlrev_b32_e32 v226, 16, v211
	v_and_b32_e32 v227, 0xffff0000, v211
	v_pk_fma_f32 v[14:15], v[6:7], v[14:15], v[224:225]
	v_pk_fma_f32 v[16:17], v[12:13], v[16:17], v[226:227]
	global_load_dwordx2 v[210:211], v[202:203], off
	v_lshl_add_u64 v[202:203], v[202:203], 0, v[196:197]
	s_waitcnt vmcnt(14)
; #define GAS __attribute__((address_space(1)))
; __device__ __forceinline__ unsigned cvt_pk_bf16(float lo, float hi) { unsigned r; asm volatile("v_cvt_pk_bf16_f32 %0, %1, %2" : "=v"(r) : "v"(lo), "v"(hi)); return r; }
; __device__ __forceinline__ void p3_scan(Frame& F) {
;     ...
;         for (int s = 0; s < NCH; ++s) { const int n = dir ? (NCH - 1 - s) : s;
;             const v2u kw = *(const GAS v2u*)(kvT + (((size_t)dh * NCH + n) * 256 + dv) * 256 + dk4 * 4); const f32x4 kv = (f32x4){bf_lo(kw.x), bf_hi(kw.x), bf_lo(kw.y), bf_hi(kw.y)};
;             v2u w; w.x = cvt_pk_bf16(S[0], S[1]); w.y = cvt_pk_bf16(S[2], S[3]);
;             *(GAS v2u*)(Bcat + ((size_t)(h * NCH + n) * 256 + dv) * CAT + 256 + dir * 256 + dk4 * 4) = w;
;             S = S * cd + kv; }
	v_cvt_pk_bf16_f32 v222, v14, v15
	v_cvt_pk_bf16_f32 v223, v16, v17
	global_store_dwordx2 v[204:205], v[222:223], off offset:512
	v_lshl_add_u64 v[204:205], v[204:205], 0, v[198:199]
	v_lshlrev_b32_e32 v224, 16, v212
	v_and_b32_e32 v225, 0xffff0000, v212
	v_lshlrev_b32_e32 v226, 16, v213
	v_and_b32_e32 v227, 0xffff0000, v213
	v_pk_fma_f32 v[14:15], v[6:7], v[14:15], v[224:225]
	v_pk_fma_f32 v[16:17], v[12:13], v[16:17], v[226:227]
	global_load_dwordx2 v[212:213], v[202:203], off
	v_lshl_add_u64 v[202:203], v[202:203], 0, v[196:197]
	s_waitcnt vmcnt(14)
	v_cvt_pk_bf16_f32 v222, v14, v15
	v_cvt_pk_bf16_f32 v223, v16, v17
	global_store_dwordx2 v[204:205], v[222:223], off offset:512
	v_lshl_add_u64 v[204:205], v[204:205], 0, v[198:199]
	v_lshlrev_b32_e32 v224, 16, v214
	v_and_b32_e32 v225, 0xffff0000, v214
	v_lshlrev_b32_e32 v226, 16, v215
	v_and_b32_e32 v227, 0xffff0000, v215
	v_pk_fma_f32 v[14:15], v[6:7], v[14:15], v[224:225]
	v_pk_fma_f32 v[16:17], v[12:13], v[16:17], v[226:227]
	global_load_dwordx2 v[214:215], v[202:203], off
	v_lshl_add_u64 v[202:203], v[202:203], 0, v[196:197]
	s_waitcnt vmcnt(14)
	v_cvt_pk_bf16_f32 v222, v14, v15
	v_cvt_pk_bf16_f32 v223, v16, v17
	global_store_dwordx2 v[204:205], v[222:223], off offset:512
	v_lshl_add_u64 v[204:205], v[204:205], 0, v[198:199]
	v_lshlrev_b32_e32 v224, 16, v216
	v_and_b32_e32 v225, 0xffff0000, v216
	v_lshlrev_b32_e32 v226, 16, v217
	v_and_b32_e32 v227, 0xffff0000, v217
	v_pk_fma_f32 v[14:15], v[6:7], v[14:15], v[224:225]
	v_pk_fma_f32 v[16:17], v[12:13], v[16:17], v[226:227]
	global_load_dwordx2 v[216:217], v[202:203], off
	v_lshl_add_u64 v[202:203], v[202:203], 0, v[196:197]
	s_waitcnt vmcnt(14)
	v_cvt_pk_bf16_f32 v222, v14, v15
	v_cvt_pk_bf16_f32 v223, v16, v17
	global_store_dwordx2 v[204:205], v[222:223], off offset:512
	v_lshl_add_u64 v[204:205], v[204:205], 0, v[198:199]
	v_lshlrev_b32_e32 v224, 16, v218
	v_and_b32_e32 v225, 0xffff0000, v218
	v_lshlrev_b32_e32 v226, 16, v219
	v_and_b32_e32 v227, 0xffff0000, v219
	v_pk_fma_f32 v[14:15], v[6:7], v[14:15], v[224:225]
	v_pk_fma_f32 v[16:17], v[12:13], v[16:17], v[226:227]
	global_load_dwordx2 v[218:219], v[202:203], off
	v_lshl_add_u64 v[202:203], v[202:203], 0, v[196:197]
	s_waitcnt vmcnt(14)
	v_cvt_pk_bf16_f32 v222, v14, v15
	v_cvt_pk_bf16_f32 v223, v16, v17
	global_store_dwordx2 v[204:205], v[222:223], off offset:512
	v_lshl_add_u64 v[204:205], v[204:205], 0, v[198:199]
	v_lshlrev_b32_e32 v224, 16, v220
	v_and_b32_e32 v225, 0xffff0000, v220
	v_lshlrev_b32_e32 v226, 16, v221
	v_and_b32_e32 v227, 0xffff0000, v221
	v_pk_fma_f32 v[14:15], v[6:7], v[14:15], v[224:225]
	v_pk_fma_f32 v[16:17], v[12:13], v[16:17], v[226:227]
	global_load_dwordx2 v[220:221], v[202:203], off
	v_lshl_add_u64 v[202:203], v[202:203], 0, v[196:197]
	s_waitcnt vmcnt(14)
	v_cvt_pk_bf16_f32 v222, v14, v15
	v_cvt_pk_bf16_f32 v223, v16, v17
	global_store_dwordx2 v[204:205], v[222:223], off offset:512
	v_lshl_add_u64 v[204:205], v[204:205], 0, v[198:199]
	v_lshlrev_b32_e32 v224, 16, v206
	v_and_b32_e32 v225, 0xffff0000, v206
	v_lshlrev_b32_e32 v226, 16, v207
	v_and_b32_e32 v227, 0xffff0000, v207
	v_pk_fma_f32 v[14:15], v[6:7], v[14:15], v[224:225]
	v_pk_fma_f32 v[16:17], v[12:13], v[16:17], v[226:227]
	global_load_dwordx2 v[206:207], v[202:203], off
	v_lshl_add_u64 v[202:203], v[202:203], 0, v[196:197]
	s_waitcnt vmcnt(14)
	v_cvt_pk_bf16_f32 v222, v14, v15
	v_cvt_pk_bf16_f32 v223, v16, v17
	global_store_dwordx2 v[204:205], v[222:223], off offset:512
	v_lshl_add_u64 v[204:205], v[204:205], 0, v[198:199]
	v_lshlrev_b32_e32 v224, 16, v208
	v_and_b32_e32 v225, 0xffff0000, v208
	v_lshlrev_b32_e32 v226, 16, v209
	v_and_b32_e32 v227, 0xffff0000, v209
	v_pk_fma_f32 v[14:15], v[6:7], v[14:15], v[224:225]
	v_pk_fma_f32 v[16:17], v[12:13], v[16:17], v[226:227]
	global_load_dwordx2 v[208:209], v[202:203], off
	v_lshl_add_u64 v[202:203], v[202:203], 0, v[196:197]
	s_waitcnt vmcnt(14)
	v_cvt_pk_bf16_f32 v222, v14, v15
	v_cvt_pk_bf16_f32 v223, v16, v17
	global_store_dwordx2 v[204:205], v[222:223], off offset:512
	v_lshl_add_u64 v[204:205], v[204:205], 0, v[198:199]
	v_lshlrev_b32_e32 v224, 16, v210
	v_and_b32_e32 v225, 0xffff0000, v210
	v_lshlrev_b32_e32 v226, 16, v211
	v_and_b32_e32 v227, 0xffff0000, v211
	v_pk_fma_f32 v[14:15], v[6:7], v[14:15], v[224:225]
	v_pk_fma_f32 v[16:17], v[12:13], v[16:17], v[226:227]
	global_load_dwordx2 v[210:211], v[202:203], off
	v_lshl_add_u64 v[202:203], v[202:203], 0, v[196:197]
	s_waitcnt vmcnt(14)
	v_cvt_pk_bf16_f32 v222, v14, v15
	v_cvt_pk_bf16_f32 v223, v16, v17
	global_store_dwordx2 v[204:205], v[222:223], off offset:512
	v_lshl_add_u64 v[204:205], v[204:205], 0, v[198:199]
	v_lshlrev_b32_e32 v224, 16, v212
	v_and_b32_e32 v225, 0xffff0000, v212
	v_lshlrev_b32_e32 v226, 16, v213
	v_and_b32_e32 v227, 0xffff0000, v213
	v_pk_fma_f32 v[14:15], v[6:7], v[14:15], v[224:225]
	v_pk_fma_f32 v[16:17], v[12:13], v[16:17], v[226:227]
	global_load_dwordx2 v[212:213], v[202:203], off
	v_lshl_add_u64 v[202:203], v[202:203], 0, v[196:197]
	s_waitcnt vmcnt(14)
	v_cvt_pk_bf16_f32 v222, v14, v15
	v_cvt_pk_bf16_f32 v223, v16, v17
	global_store_dwordx2 v[204:205], v[222:223], off offset:512
	v_lshl_add_u64 v[204:205], v[204:205], 0, v[198:199]
	v_lshlrev_b32_e32 v224, 16, v214
	v_and_b32_e32 v225, 0xffff0000, v214
	v_lshlrev_b32_e32 v226, 16, v215
	v_and_b32_e32 v227, 0xffff0000, v215
	v_pk_fma_f32 v[14:15], v[6:7], v[14:15], v[224:225]
	v_pk_fma_f32 v[16:17], v[12:13], v[16:17], v[226:227]
	global_load_dwordx2 v[214:215], v[202:203], off
	v_lshl_add_u64 v[202:203], v[202:203], 0, v[196:197]
	s_waitcnt vmcnt(14)
; #define GAS __attribute__((address_space(1)))
; __device__ __forceinline__ unsigned cvt_pk_bf16(float lo, float hi) { unsigned r; asm volatile("v_cvt_pk_bf16_f32 %0, %1, %2" : "=v"(r) : "v"(lo), "v"(hi)); return r; }
; __device__ __forceinline__ void p3_scan(Frame& F) {
;     ...
;         for (int s = 0; s < NCH; ++s) { const int n = dir ? (NCH - 1 - s) : s;
;             const v2u kw = *(const GAS v2u*)(kvT + (((size_t)dh * NCH + n) * 256 + dv) * 256 + dk4 * 4); const f32x4 kv = (f32x4){bf_lo(kw.x), bf_hi(kw.x), bf_lo(kw.y), bf_hi(kw.y)};
;             v2u w; w.x = cvt_pk_bf16(S[0], S[1]); w.y = cvt_pk_bf16(S[2], S[3]);
;             *(GAS v2u*)(Bcat + ((size_t)(h * NCH + n) * 256 + dv) * CAT + 256 + dir * 256 + dk4 * 4) = w;
;             S = S * cd + kv; }
	v_cvt_pk_bf16_f32 v222, v14, v15
	v_cvt_pk_bf16_f32 v223, v16, v17
	global_store_dwordx2 v[204:205], v[222:223], off offset:512
	v_lshl_add_u64 v[204:205], v[204:205], 0, v[198:199]
	v_lshlrev_b32_e32 v224, 16, v216
	v_and_b32_e32 v225, 0xffff0000, v216
	v_lshlrev_b32_e32 v226, 16, v217
	v_and_b32_e32 v227, 0xffff0000, v217
	v_pk_fma_f32 v[14:15], v[6:7], v[14:15], v[224:225]
	v_pk_fma_f32 v[16:17], v[12:13], v[16:17], v[226:227]
	global_load_dwordx2 v[216:217], v[202:203], off
	v_lshl_add_u64 v[202:203], v[202:203], 0, v[196:197]
	s_waitcnt vmcnt(14)
	v_cvt_pk_bf16_f32 v222, v14, v15
	v_cvt_pk_bf16_f32 v223, v16, v17
	global_store_dwordx2 v[204:205], v[222:223], off offset:512
	v_lshl_add_u64 v[204:205], v[204:205], 0, v[198:199]
	v_lshlrev_b32_e32 v224, 16, v218
	v_and_b32_e32 v225, 0xffff0000, v218
	v_lshlrev_b32_e32 v226, 16, v219
	v_and_b32_e32 v227, 0xffff0000, v219
	v_pk_fma_f32 v[14:15], v[6:7], v[14:15], v[224:225]
	v_pk_fma_f32 v[16:17], v[12:13], v[16:17], v[226:227]
	global_load_dwordx2 v[218:219], v[202:203], off
	v_lshl_add_u64 v[202:203], v[202:203], 0, v[196:197]
	s_waitcnt vmcnt(14)
	v_cvt_pk_bf16_f32 v222, v14, v15
	v_cvt_pk_bf16_f32 v223, v16, v17
	global_store_dwordx2 v[204:205], v[222:223], off offset:512
	v_lshl_add_u64 v[204:205], v[204:205], 0, v[198:199]
	v_lshlrev_b32_e32 v224, 16, v220
	v_and_b32_e32 v225, 0xffff0000, v220
	v_lshlrev_b32_e32 v226, 16, v221
	v_and_b32_e32 v227, 0xffff0000, v221
	v_pk_fma_f32 v[14:15], v[6:7], v[14:15], v[224:225]
	v_pk_fma_f32 v[16:17], v[12:13], v[16:17], v[226:227]
	global_load_dwordx2 v[220:221], v[202:203], off
	v_lshl_add_u64 v[202:203], v[202:203], 0, v[196:197]
	s_waitcnt vmcnt(14)
	v_cvt_pk_bf16_f32 v222, v14, v15
	v_cvt_pk_bf16_f32 v223, v16, v17
	global_store_dwordx2 v[204:205], v[222:223], off offset:512
	v_lshl_add_u64 v[204:205], v[204:205], 0, v[198:199]
	v_lshlrev_b32_e32 v224, 16, v206
	v_and_b32_e32 v225, 0xffff0000, v206
	v_lshlrev_b32_e32 v226, 16, v207
	v_and_b32_e32 v227, 0xffff0000, v207
	v_pk_fma_f32 v[14:15], v[6:7], v[14:15], v[224:225]
	v_pk_fma_f32 v[16:17], v[12:13], v[16:17], v[226:227]
	global_load_dwordx2 v[206:207], v[202:203], off
	v_lshl_add_u64 v[202:203], v[202:203], 0, v[196:197]
	s_waitcnt vmcnt(14)
	v_cvt_pk_bf16_f32 v222, v14, v15
	v_cvt_pk_bf16_f32 v223, v16, v17
	global_store_dwordx2 v[204:205], v[222:223], off offset:512
	v_lshl_add_u64 v[204:205], v[204:205], 0, v[198:199]
	v_lshlrev_b32_e32 v224, 16, v208
	v_and_b32_e32 v225, 0xffff0000, v208
	v_lshlrev_b32_e32 v226, 16, v209
	v_and_b32_e32 v227, 0xffff0000, v209
	v_pk_fma_f32 v[14:15], v[6:7], v[14:15], v[224:225]
	v_pk_fma_f32 v[16:17], v[12:13], v[16:17], v[226:227]
	global_load_dwordx2 v[208:209], v[202:203], off
	v_lshl_add_u64 v[202:203], v[202:203], 0, v[196:197]
	s_waitcnt vmcnt(14)
	v_cvt_pk_bf16_f32 v222, v14, v15
	v_cvt_pk_bf16_f32 v223, v16, v17
	global_store_dwordx2 v[204:205], v[222:223], off offset:512
	v_lshl_add_u64 v[204:205], v[204:205], 0, v[198:199]
	v_lshlrev_b32_e32 v224, 16, v210
	v_and_b32_e32 v225, 0xffff0000, v210
	v_lshlrev_b32_e32 v226, 16, v211
	v_and_b32_e32 v227, 0xffff0000, v211
	v_pk_fma_f32 v[14:15], v[6:7], v[14:15], v[224:225]
	v_pk_fma_f32 v[16:17], v[12:13], v[16:17], v[226:227]
	global_load_dwordx2 v[210:211], v[202:203], off
	v_lshl_add_u64 v[202:203], v[202:203], 0, v[196:197]
	s_waitcnt vmcnt(14)
	v_cvt_pk_bf16_f32 v222, v14, v15
	v_cvt_pk_bf16_f32 v223, v16, v17
	global_store_dwordx2 v[204:205], v[222:223], off offset:512
	v_lshl_add_u64 v[204:205], v[204:205], 0, v[198:199]
	v_lshlrev_b32_e32 v224, 16, v212
	v_and_b32_e32 v225, 0xffff0000, v212
	v_lshlrev_b32_e32 v226, 16, v213
	v_and_b32_e32 v227, 0xffff0000, v213
	v_pk_fma_f32 v[14:15], v[6:7], v[14:15], v[224:225]
	v_pk_fma_f32 v[16:17], v[12:13], v[16:17], v[226:227]
	global_load_dwordx2 v[212:213], v[202:203], off
	v_lshl_add_u64 v[202:203], v[202:203], 0, v[196:197]
	s_waitcnt vmcnt(14)
	v_cvt_pk_bf16_f32 v222, v14, v15
	v_cvt_pk_bf16_f32 v223, v16, v17
	global_store_dwordx2 v[204:205], v[222:223], off offset:512
	v_lshl_add_u64 v[204:205], v[204:205], 0, v[198:199]
	v_lshlrev_b32_e32 v224, 16, v214
	v_and_b32_e32 v225, 0xffff0000, v214
	v_lshlrev_b32_e32 v226, 16, v215
	v_and_b32_e32 v227, 0xffff0000, v215
	v_pk_fma_f32 v[14:15], v[6:7], v[14:15], v[224:225]
	v_pk_fma_f32 v[16:17], v[12:13], v[16:17], v[226:227]
	global_load_dwordx2 v[214:215], v[202:203], off
	v_lshl_add_u64 v[202:203], v[202:203], 0, v[196:197]
	s_waitcnt vmcnt(14)
	v_cvt_pk_bf16_f32 v222, v14, v15
	v_cvt_pk_bf16_f32 v223, v16, v17
	global_store_dwordx2 v[204:205], v[222:223], off offset:512
	v_lshl_add_u64 v[204:205], v[204:205], 0, v[198:199]
	v_lshlrev_b32_e32 v224, 16, v216
	v_and_b32_e32 v225, 0xffff0000, v216
	v_lshlrev_b32_e32 v226, 16, v217
	v_and_b32_e32 v227, 0xffff0000, v217
	v_pk_fma_f32 v[14:15], v[6:7], v[14:15], v[224:225]
	v_pk_fma_f32 v[16:17], v[12:13], v[16:17], v[226:227]
	global_load_dwordx2 v[216:217], v[202:203], off
	v_lshl_add_u64 v[202:203], v[202:203], 0, v[196:197]
	s_waitcnt vmcnt(14)
	v_cvt_pk_bf16_f32 v222, v14, v15
	v_cvt_pk_bf16_f32 v223, v16, v17
	global_store_dwordx2 v[204:205], v[222:223], off offset:512
	v_lshl_add_u64 v[204:205], v[204:205], 0, v[198:199]
	v_lshlrev_b32_e32 v224, 16, v218
	v_and_b32_e32 v225, 0xffff0000, v218
	v_lshlrev_b32_e32 v226, 16, v219
	v_and_b32_e32 v227, 0xffff0000, v219
	v_pk_fma_f32 v[14:15], v[6:7], v[14:15], v[224:225]
	v_pk_fma_f32 v[16:17], v[12:13], v[16:17], v[226:227]
	global_load_dwordx2 v[218:219], v[202:203], off
	v_lshl_add_u64 v[202:203], v[202:203], 0, v[196:197]
	s_waitcnt vmcnt(14)
; #define GAS __attribute__((address_space(1)))
; __device__ __forceinline__ unsigned cvt_pk_bf16(float lo, float hi) { unsigned r; asm volatile("v_cvt_pk_bf16_f32 %0, %1, %2" : "=v"(r) : "v"(lo), "v"(hi)); return r; }
; __device__ __forceinline__ void p3_scan(Frame& F) {
;     ...
;         for (int s = 0; s < NCH; ++s) { const int n = dir ? (NCH - 1 - s) : s;
;             const v2u kw = *(const GAS v2u*)(kvT + (((size_t)dh * NCH + n) * 256 + dv) * 256 + dk4 * 4); const f32x4 kv = (f32x4){bf_lo(kw.x), bf_hi(kw.x), bf_lo(kw.y), bf_hi(kw.y)};
;             v2u w; w.x = cvt_pk_bf16(S[0], S[1]); w.y = cvt_pk_bf16(S[2], S[3]);
;             *(GAS v2u*)(Bcat + ((size_t)(h * NCH + n) * 256 + dv) * CAT + 256 + dir * 256 + dk4 * 4) = w;
;             S = S * cd + kv; }
	v_cvt_pk_bf16_f32 v222, v14, v15
	v_cvt_pk_bf16_f32 v223, v16, v17
	global_store_dwordx2 v[204:205], v[222:223], off offset:512
	v_lshl_add_u64 v[204:205], v[204:205], 0, v[198:199]
	v_lshlrev_b32_e32 v224, 16, v220
	v_and_b32_e32 v225, 0xffff0000, v220
	v_lshlrev_b32_e32 v226, 16, v221
	v_and_b32_e32 v227, 0xffff0000, v221
	v_pk_fma_f32 v[14:15], v[6:7], v[14:15], v[224:225]
	v_pk_fma_f32 v[16:17], v[12:13], v[16:17], v[226:227]
	global_load_dwordx2 v[220:221], v[202:203], off
	v_lshl_add_u64 v[202:203], v[202:203], 0, v[196:197]
	s_waitcnt vmcnt(14)
	v_cvt_pk_bf16_f32 v222, v14, v15
	v_cvt_pk_bf16_f32 v223, v16, v17
	global_store_dwordx2 v[204:205], v[222:223], off offset:512
	v_lshl_add_u64 v[204:205], v[204:205], 0, v[198:199]
	v_lshlrev_b32_e32 v224, 16, v206
	v_and_b32_e32 v225, 0xffff0000, v206
	v_lshlrev_b32_e32 v226, 16, v207
	v_and_b32_e32 v227, 0xffff0000, v207
	v_pk_fma_f32 v[14:15], v[6:7], v[14:15], v[224:225]
	v_pk_fma_f32 v[16:17], v[12:13], v[16:17], v[226:227]
	global_load_dwordx2 v[206:207], v[202:203], off
	v_lshl_add_u64 v[202:203], v[202:203], 0, v[196:197]
	s_waitcnt vmcnt(14)
	v_cvt_pk_bf16_f32 v222, v14, v15
	v_cvt_pk_bf16_f32 v223, v16, v17
	global_store_dwordx2 v[204:205], v[222:223], off offset:512
	v_lshl_add_u64 v[204:205], v[204:205], 0, v[198:199]
	v_lshlrev_b32_e32 v224, 16, v208
	v_and_b32_e32 v225, 0xffff0000, v208
	v_lshlrev_b32_e32 v226, 16, v209
	v_and_b32_e32 v227, 0xffff0000, v209
	v_pk_fma_f32 v[14:15], v[6:7], v[14:15], v[224:225]
	v_pk_fma_f32 v[16:17], v[12:13], v[16:17], v[226:227]
	global_load_dwordx2 v[208:209], v[202:203], off
	v_lshl_add_u64 v[202:203], v[202:203], 0, v[196:197]
	s_waitcnt vmcnt(14)
	v_cvt_pk_bf16_f32 v222, v14, v15
	v_cvt_pk_bf16_f32 v223, v16, v17
	global_store_dwordx2 v[204:205], v[222:223], off offset:512
	v_lshl_add_u64 v[204:205], v[204:205], 0, v[198:199]
	v_lshlrev_b32_e32 v224, 16, v210
	v_and_b32_e32 v225, 0xffff0000, v210
	v_lshlrev_b32_e32 v226, 16, v211
	v_and_b32_e32 v227, 0xffff0000, v211
	v_pk_fma_f32 v[14:15], v[6:7], v[14:15], v[224:225]
	v_pk_fma_f32 v[16:17], v[12:13], v[16:17], v[226:227]
	global_load_dwordx2 v[210:211], v[202:203], off
	v_lshl_add_u64 v[202:203], v[202:203], 0, v[196:197]
	s_waitcnt vmcnt(14)
	v_cvt_pk_bf16_f32 v222, v14, v15
	v_cvt_pk_bf16_f32 v223, v16, v17
	global_store_dwordx2 v[204:205], v[222:223], off offset:512
	v_lshl_add_u64 v[204:205], v[204:205], 0, v[198:199]
	v_lshlrev_b32_e32 v224, 16, v212
	v_and_b32_e32 v225, 0xffff0000, v212
	v_lshlrev_b32_e32 v226, 16, v213
	v_and_b32_e32 v227, 0xffff0000, v213
	v_pk_fma_f32 v[14:15], v[6:7], v[14:15], v[224:225]
	v_pk_fma_f32 v[16:17], v[12:13], v[16:17], v[226:227]
	global_load_dwordx2 v[212:213], v[202:203], off
	v_lshl_add_u64 v[202:203], v[202:203], 0, v[196:197]
	s_waitcnt vmcnt(14)
	v_cvt_pk_bf16_f32 v222, v14, v15
	v_cvt_pk_bf16_f32 v223, v16, v17
	global_store_dwordx2 v[204:205], v[222:223], off offset:512
	v_lshl_add_u64 v[204:205], v[204:205], 0, v[198:199]
	v_lshlrev_b32_e32 v224, 16, v214
	v_and_b32_e32 v225, 0xffff0000, v214
	v_lshlrev_b32_e32 v226, 16, v215
	v_and_b32_e32 v227, 0xffff0000, v215
	v_pk_fma_f32 v[14:15], v[6:7], v[14:15], v[224:225]
	v_pk_fma_f32 v[16:17], v[12:13], v[16:17], v[226:227]
	global_load_dwordx2 v[214:215], v[202:203], off
	v_lshl_add_u64 v[202:203], v[202:203], 0, v[196:197]
	s_waitcnt vmcnt(14)
	v_cvt_pk_bf16_f32 v222, v14, v15
	v_cvt_pk_bf16_f32 v223, v16, v17
	global_store_dwordx2 v[204:205], v[222:223], off offset:512
	v_lshl_add_u64 v[204:205], v[204:205], 0, v[198:199]
	v_lshlrev_b32_e32 v224, 16, v216
	v_and_b32_e32 v225, 0xffff0000, v216
	v_lshlrev_b32_e32 v226, 16, v217
	v_and_b32_e32 v227, 0xffff0000, v217
	v_pk_fma_f32 v[14:15], v[6:7], v[14:15], v[224:225]
	v_pk_fma_f32 v[16:17], v[12:13], v[16:17], v[226:227]
	global_load_dwordx2 v[216:217], v[202:203], off
	v_lshl_add_u64 v[202:203], v[202:203], 0, v[196:197]
	s_waitcnt vmcnt(14)
	v_cvt_pk_bf16_f32 v222, v14, v15
	v_cvt_pk_bf16_f32 v223, v16, v17
	global_store_dwordx2 v[204:205], v[222:223], off offset:512
	v_lshl_add_u64 v[204:205], v[204:205], 0, v[198:199]
	v_lshlrev_b32_e32 v224, 16, v218
	v_and_b32_e32 v225, 0xffff0000, v218
	v_lshlrev_b32_e32 v226, 16, v219
	v_and_b32_e32 v227, 0xffff0000, v219
	v_pk_fma_f32 v[14:15], v[6:7], v[14:15], v[224:225]
	v_pk_fma_f32 v[16:17], v[12:13], v[16:17], v[226:227]
	global_load_dwordx2 v[218:219], v[202:203], off
	v_lshl_add_u64 v[202:203], v[202:203], 0, v[196:197]
	s_waitcnt vmcnt(14)
; #define GAS __attribute__((address_space(1)))
; __device__ __forceinline__ unsigned cvt_pk_bf16(float lo, float hi) { unsigned r; asm volatile("v_cvt_pk_bf16_f32 %0, %1, %2" : "=v"(r) : "v"(lo), "v"(hi)); return r; }
; __device__ __forceinline__ void p3_scan(Frame& F) {
;     ...
;         for (int s = 0; s < NCH; ++s) { const int n = dir ? (NCH - 1 - s) : s;
;             const v2u kw = *(const GAS v2u*)(kvT + (((size_t)dh * NCH + n) * 256 + dv) * 256 + dk4 * 4); const f32x4 kv = (f32x4){bf_lo(kw.x), bf_hi(kw.x), bf_lo(kw.y), bf_hi(kw.y)};
;             v2u w; w.x = cvt_pk_bf16(S[0], S[1]); w.y = cvt_pk_bf16(S[2], S[3]);
;             *(GAS v2u*)(Bcat + ((size_t)(h * NCH + n) * 256 + dv) * CAT + 256 + dir * 256 + dk4 * 4) = w;
;             S = S * cd + kv; }
;     }
	v_cvt_pk_bf16_f32 v222, v14, v15
	v_cvt_pk_bf16_f32 v223, v16, v17
	global_store_dwordx2 v[204:205], v[222:223], off offset:512
	v_lshl_add_u64 v[204:205], v[204:205], 0, v[198:199]
	v_lshlrev_b32_e32 v224, 16, v220
	v_and_b32_e32 v225, 0xffff0000, v220
	v_lshlrev_b32_e32 v226, 16, v221
	v_and_b32_e32 v227, 0xffff0000, v221
	v_pk_fma_f32 v[14:15], v[6:7], v[14:15], v[224:225]
	v_pk_fma_f32 v[16:17], v[12:13], v[16:17], v[226:227]
	global_load_dwordx2 v[220:221], v[202:203], off
	v_lshl_add_u64 v[202:203], v[202:203], 0, v[196:197]
	s_waitcnt vmcnt(14)
	v_cvt_pk_bf16_f32 v222, v14, v15
	v_cvt_pk_bf16_f32 v223, v16, v17
	global_store_dwordx2 v[204:205], v[222:223], off offset:512
	v_lshl_add_u64 v[204:205], v[204:205], 0, v[198:199]
	v_lshlrev_b32_e32 v224, 16, v206
	v_and_b32_e32 v225, 0xffff0000, v206
	v_lshlrev_b32_e32 v226, 16, v207
	v_and_b32_e32 v227, 0xffff0000, v207
	v_pk_fma_f32 v[14:15], v[6:7], v[14:15], v[224:225]
	v_pk_fma_f32 v[16:17], v[12:13], v[16:17], v[226:227]
	s_waitcnt vmcnt(13)
	v_cvt_pk_bf16_f32 v222, v14, v15
	v_cvt_pk_bf16_f32 v223, v16, v17
	global_store_dwordx2 v[204:205], v[222:223], off offset:512
	v_lshl_add_u64 v[204:205], v[204:205], 0, v[198:199]
	v_lshlrev_b32_e32 v224, 16, v208
	v_and_b32_e32 v225, 0xffff0000, v208
	v_lshlrev_b32_e32 v226, 16, v209
	v_and_b32_e32 v227, 0xffff0000, v209
	v_pk_fma_f32 v[14:15], v[6:7], v[14:15], v[224:225]
	v_pk_fma_f32 v[16:17], v[12:13], v[16:17], v[226:227]
	s_waitcnt vmcnt(12)
	v_cvt_pk_bf16_f32 v222, v14, v15
	v_cvt_pk_bf16_f32 v223, v16, v17
	global_store_dwordx2 v[204:205], v[222:223], off offset:512
	v_lshl_add_u64 v[204:205], v[204:205], 0, v[198:199]
	v_lshlrev_b32_e32 v224, 16, v210
	v_and_b32_e32 v225, 0xffff0000, v210
	v_lshlrev_b32_e32 v226, 16, v211
	v_and_b32_e32 v227, 0xffff0000, v211
	v_pk_fma_f32 v[14:15], v[6:7], v[14:15], v[224:225]
	v_pk_fma_f32 v[16:17], v[12:13], v[16:17], v[226:227]
	s_waitcnt vmcnt(11)
	v_cvt_pk_bf16_f32 v222, v14, v15
	v_cvt_pk_bf16_f32 v223, v16, v17
	global_store_dwordx2 v[204:205], v[222:223], off offset:512
	v_lshl_add_u64 v[204:205], v[204:205], 0, v[198:199]
	v_lshlrev_b32_e32 v224, 16, v212
	v_and_b32_e32 v225, 0xffff0000, v212
	v_lshlrev_b32_e32 v226, 16, v213
	v_and_b32_e32 v227, 0xffff0000, v213
	v_pk_fma_f32 v[14:15], v[6:7], v[14:15], v[224:225]
	v_pk_fma_f32 v[16:17], v[12:13], v[16:17], v[226:227]
	s_waitcnt vmcnt(10)
	v_cvt_pk_bf16_f32 v222, v14, v15
	v_cvt_pk_bf16_f32 v223, v16, v17
	global_store_dwordx2 v[204:205], v[222:223], off offset:512
	v_lshl_add_u64 v[204:205], v[204:205], 0, v[198:199]
	v_lshlrev_b32_e32 v224, 16, v214
	v_and_b32_e32 v225, 0xffff0000, v214
	v_lshlrev_b32_e32 v226, 16, v215
	v_and_b32_e32 v227, 0xffff0000, v215
	v_pk_fma_f32 v[14:15], v[6:7], v[14:15], v[224:225]
	v_pk_fma_f32 v[16:17], v[12:13], v[16:17], v[226:227]
	s_waitcnt vmcnt(9)
	v_cvt_pk_bf16_f32 v222, v14, v15
	v_cvt_pk_bf16_f32 v223, v16, v17
	global_store_dwordx2 v[204:205], v[222:223], off offset:512
	v_lshl_add_u64 v[204:205], v[204:205], 0, v[198:199]
	v_lshlrev_b32_e32 v224, 16, v216
	v_and_b32_e32 v225, 0xffff0000, v216
	v_lshlrev_b32_e32 v226, 16, v217
	v_and_b32_e32 v227, 0xffff0000, v217
	v_pk_fma_f32 v[14:15], v[6:7], v[14:15], v[224:225]
	v_pk_fma_f32 v[16:17], v[12:13], v[16:17], v[226:227]
	s_waitcnt vmcnt(8)
	v_cvt_pk_bf16_f32 v222, v14, v15
	v_cvt_pk_bf16_f32 v223, v16, v17
	global_store_dwordx2 v[204:205], v[222:223], off offset:512
	v_lshl_add_u64 v[204:205], v[204:205], 0, v[198:199]
	v_lshlrev_b32_e32 v224, 16, v218
	v_and_b32_e32 v225, 0xffff0000, v218
	v_lshlrev_b32_e32 v226, 16, v219
	v_and_b32_e32 v227, 0xffff0000, v219
	v_pk_fma_f32 v[14:15], v[6:7], v[14:15], v[224:225]
	v_pk_fma_f32 v[16:17], v[12:13], v[16:17], v[226:227]
	s_waitcnt vmcnt(7)
	v_cvt_pk_bf16_f32 v222, v14, v15
	v_cvt_pk_bf16_f32 v223, v16, v17
	global_store_dwordx2 v[204:205], v[222:223], off offset:512
	v_lshl_add_u64 v[204:205], v[204:205], 0, v[198:199]
	v_lshlrev_b32_e32 v224, 16, v220
	v_and_b32_e32 v225, 0xffff0000, v220
	v_lshlrev_b32_e32 v226, 16, v221
	v_and_b32_e32 v227, 0xffff0000, v221
	v_pk_fma_f32 v[14:15], v[6:7], v[14:15], v[224:225]
	v_pk_fma_f32 v[16:17], v[12:13], v[16:17], v[226:227]
	s_mov_b32 s21, -4
	s_mov_b32 s22, 64
	v_add_u32_e32 v18, s2, v18
	v_cmp_lt_i32_e32 vcc, s20, v18
	s_or_b64 s[34:35], vcc, s[34:35]
	s_andn2_b64 exec, exec, s[34:35]
	s_cbranch_execnz .LBB0_831
